# P0 block-diagonal gate-weight build: 8 strided loads issued up-front instead of load/wait per iteration; P17 router-weight staging loop unrolled x4 with 12 loads in flight
# speedup vs baseline: 1.0009x; 1.0009x over previous
; __device__ __forceinline__ unsigned cvtpk(float lo, float hi) { unsigned r; asm volatile("v_cvt_pk_bf16_f32 %0, %1, %2" : "=v"(r) : "v"(lo), "v"(hi)); return r; }
; __global__ void __launch_bounds__(NTHREADS, 2) fwd_kernel(Args args) {
;     ...
;         { bf16_t* Wg = (bf16_t*)(ws + W_GATE); const float* wa = args.in[I_RGWA]; const float* wx = args.in[I_RGWX];
;           for (int idx = gtid; idx < 16 * 256 * 256; idx += NGT) { const int h = idx >> 16, n = (idx >> 8) & 255, k = idx & 255, kl = k - 128 * (h & 1);
;               float v = 0.f; if (kl >= 0 && kl < 128) v = (n < 128) ? wa[((size_t)h * 128 + kl) * 128 + n] : wx[((size_t)h * 128 + kl) * 128 + (n - 128)];
;               Wg[idx] = (bf16_t)(cvtpk(v, 0.f) & 0xffffu); } }
.LBB0_62:
	s_or_b64 exec, exec, s[6:7]
	s_mov_b32 s0, 0x100000
	v_cmp_gt_i32_e32 vcc, s0, v6
	s_and_saveexec_b64 s[6:7], vcc
	s_cbranch_execz .LBB0_71
	s_cmp_eq_u32 s4, 0x20000
	s_cbranch_scc0 .Lwg_orig
	v_lshl_add_u64 v[2:3], v[6:7], 1, s[70:71]
	s_mov_b64 s[0:1], 0x1800000
	v_lshl_add_u64 v[2:3], v[2:3], 0, s[0:1]
	s_ashr_i32 s5, s4, 31
	s_lshl_b64 s[10:11], s[4:5], 1
	v_readlane_b32 s52, v251, 21
	v_readlane_b32 s53, v251, 22
	v_readlane_b32 s56, v251, 25
	v_readlane_b32 s57, v251, 26
	v_lshrrev_b32_e32 v28, 16, v6
	v_and_b32_e32 v29, 0xff, v6
	v_lshlrev_b32_e32 v30, 7, v28
	v_sub_u32_e32 v29, v29, v30
	v_bfe_u32 v31, v6, 8, 8
	v_and_b32_e32 v32, 0x7f, v31
	v_lshlrev_b32_e32 v33, 16, v28
	v_lshl_add_u32 v33, v29, 9, v33
	v_lshl_add_u32 v33, v32, 2, v33
	v_mov_b32_e32 v34, s52
	v_mov_b32_e32 v35, s53
	v_mov_b32_e32 v36, s56
	v_mov_b32_e32 v37, s57
	v_cmp_lt_u32_e32 vcc, 0x7f, v31
	s_nop 1
	v_cndmask_b32_e32 v34, v34, v36, vcc
	v_cndmask_b32_e32 v35, v35, v37, vcc
	v_mov_b32_e32 v5, 0
	v_add_co_u32_e32 v34, vcc, v34, v33
	s_nop 1
	v_addc_co_u32_e32 v35, vcc, 0, v35, vcc
	v_mov_b32_e32 v20, 0
	v_mov_b32_e32 v21, 0
	v_mov_b32_e32 v22, 0
	v_mov_b32_e32 v23, 0
	v_mov_b32_e32 v24, 0
	v_mov_b32_e32 v25, 0
	v_mov_b32_e32 v26, 0
	v_mov_b32_e32 v27, 0
	s_mov_b64 s[0:1], 0x20000
	v_cmp_gt_u32_e32 vcc, 0x80, v29
	s_and_saveexec_b64 s[22:23], vcc
	global_load_dword v20, v[34:35], off
	v_lshl_add_u64 v[34:35], v[34:35], 0, s[0:1]
	global_load_dword v21, v[34:35], off
	v_lshl_add_u64 v[34:35], v[34:35], 0, s[0:1]
	global_load_dword v22, v[34:35], off
	v_lshl_add_u64 v[34:35], v[34:35], 0, s[0:1]
	global_load_dword v23, v[34:35], off
	v_lshl_add_u64 v[34:35], v[34:35], 0, s[0:1]
	global_load_dword v24, v[34:35], off
	v_lshl_add_u64 v[34:35], v[34:35], 0, s[0:1]
	global_load_dword v25, v[34:35], off
	v_lshl_add_u64 v[34:35], v[34:35], 0, s[0:1]
	global_load_dword v26, v[34:35], off
	v_lshl_add_u64 v[34:35], v[34:35], 0, s[0:1]
	global_load_dword v27, v[34:35], off
	s_or_b64 exec, exec, s[22:23]
	s_waitcnt vmcnt(0)
	v_cvt_pk_bf16_f32 v40, v20, v5
	v_cvt_pk_bf16_f32 v41, v21, v5
	v_cvt_pk_bf16_f32 v42, v22, v5
	v_cvt_pk_bf16_f32 v43, v23, v5
	v_cvt_pk_bf16_f32 v44, v24, v5
	v_cvt_pk_bf16_f32 v45, v25, v5
	v_cvt_pk_bf16_f32 v46, v26, v5
	v_cvt_pk_bf16_f32 v47, v27, v5
	global_store_short v[2:3], v40, off
	v_lshl_add_u64 v[2:3], v[2:3], 0, s[10:11]
	global_store_short v[2:3], v41, off
	v_lshl_add_u64 v[2:3], v[2:3], 0, s[10:11]
	global_store_short v[2:3], v42, off
	v_lshl_add_u64 v[2:3], v[2:3], 0, s[10:11]
	global_store_short v[2:3], v43, off
	v_lshl_add_u64 v[2:3], v[2:3], 0, s[10:11]
	global_store_short v[2:3], v44, off
	v_lshl_add_u64 v[2:3], v[2:3], 0, s[10:11]
	global_store_short v[2:3], v45, off
	v_lshl_add_u64 v[2:3], v[2:3], 0, s[10:11]
	global_store_short v[2:3], v46, off
	v_lshl_add_u64 v[2:3], v[2:3], 0, s[10:11]
	global_store_short v[2:3], v47, off
	s_branch .LBB0_71
.Lwg_orig:
	v_lshl_add_u64 v[2:3], v[6:7], 1, s[70:71]
	s_mov_b64 s[0:1], 0x1800000
	s_ashr_i32 s5, s4, 31
	s_movk_i32 s16, 0xfe00
	v_lshl_add_u64 v[2:3], v[2:3], 0, s[0:1]
	s_lshl_b64 s[10:11], s[4:5], 1
	s_mov_b64 s[14:15], 0
	s_movk_i32 s0, 0x80
	s_movk_i32 s1, 0x7f
	v_mov_b32_e32 v5, 0
	s_mov_b32 s17, -1
	s_mov_b32 s3, 0xfffff
	v_mov_b32_e32 v14, 2
	v_mov_b32_e32 v15, v6
	s_branch .LBB0_66

; __global__ void __launch_bounds__(NTHREADS, 2) fwd_kernel(Args args) {
;     ...
;         for (int d = tid; d < D; d += NTHREADS) { const float gd = gain[d]; const f32x4 a = *(const f32x4*)(wrt + (size_t)d * 8), c = *(const f32x4*)(wrt + (size_t)d * 8 + 4);
;             wr[0 * D + d] = a.x * gd; wr[1 * D + d] = a.y * gd; wr[2 * D + d] = a.z * gd; wr[3 * D + d] = a.w * gd; wr[4 * D + d] = c.x * gd; wr[5 * D + d] = c.y * gd; wr[6 * D + d] = c.z * gd; wr[7 * D + d] = c.w * gd; }
.LBB0_1183:
	global_load_dword v16, v[2:3], off
	global_load_dwordx4 v[8:11], v[4:5], off offset:-16
	global_load_dwordx4 v[12:15], v[4:5], off
	v_lshl_add_u64 v[2:3], v[2:3], 0, s[8:9]
	v_lshl_add_u64 v[4:5], v[4:5], 0, s[10:11]
	global_load_dword v48, v[2:3], off
	global_load_dwordx4 v[40:43], v[4:5], off offset:-16
	global_load_dwordx4 v[44:47], v[4:5], off
	v_lshl_add_u64 v[2:3], v[2:3], 0, s[8:9]
	v_lshl_add_u64 v[4:5], v[4:5], 0, s[10:11]
	global_load_dword v58, v[2:3], off
	global_load_dwordx4 v[50:53], v[4:5], off offset:-16
	global_load_dwordx4 v[54:57], v[4:5], off
	v_lshl_add_u64 v[2:3], v[2:3], 0, s[8:9]
	v_lshl_add_u64 v[4:5], v[4:5], 0, s[10:11]
	global_load_dword v68, v[2:3], off
	global_load_dwordx4 v[60:63], v[4:5], off offset:-16
	global_load_dwordx4 v[64:67], v[4:5], off
	s_waitcnt vmcnt(9)
	v_mul_f32_e32 v8, v16, v8
	v_mul_f32_e32 v9, v16, v9
	v_mul_f32_e32 v10, v16, v10
	v_mul_f32_e32 v11, v16, v11
	v_mul_f32_e32 v12, v16, v12
	v_mul_f32_e32 v13, v16, v13
	v_mul_f32_e32 v14, v16, v14
	v_mul_f32_e32 v15, v16, v15
	ds_write2st64_b32 v7, v8, v9 offset1:32
	ds_write2st64_b32 v7, v10, v11 offset0:64 offset1:96
	ds_write2st64_b32 v7, v12, v13 offset0:128 offset1:160
	ds_write2st64_b32 v7, v14, v15 offset0:192 offset1:224
	v_add_u32_e32 v7, 0x800, v7
	s_waitcnt vmcnt(6)
	v_mul_f32_e32 v40, v48, v40
	v_mul_f32_e32 v41, v48, v41
	v_mul_f32_e32 v42, v48, v42
	v_mul_f32_e32 v43, v48, v43
	v_mul_f32_e32 v44, v48, v44
	v_mul_f32_e32 v45, v48, v45
	v_mul_f32_e32 v46, v48, v46
	v_mul_f32_e32 v47, v48, v47
	ds_write2st64_b32 v7, v40, v41 offset1:32
	ds_write2st64_b32 v7, v42, v43 offset0:64 offset1:96
	ds_write2st64_b32 v7, v44, v45 offset0:128 offset1:160
	ds_write2st64_b32 v7, v46, v47 offset0:192 offset1:224
	v_add_u32_e32 v7, 0x800, v7
	s_waitcnt vmcnt(3)
	v_mul_f32_e32 v50, v58, v50
	v_mul_f32_e32 v51, v58, v51
	v_mul_f32_e32 v52, v58, v52
	v_mul_f32_e32 v53, v58, v53
	v_mul_f32_e32 v54, v58, v54
	v_mul_f32_e32 v55, v58, v55
	v_mul_f32_e32 v56, v58, v56
	v_mul_f32_e32 v57, v58, v57
	ds_write2st64_b32 v7, v50, v51 offset1:32
	ds_write2st64_b32 v7, v52, v53 offset0:64 offset1:96
	ds_write2st64_b32 v7, v54, v55 offset0:128 offset1:160
	ds_write2st64_b32 v7, v56, v57 offset0:192 offset1:224
	v_add_u32_e32 v7, 0x800, v7
	s_waitcnt vmcnt(0)
	v_mul_f32_e32 v60, v68, v60
	v_mul_f32_e32 v61, v68, v61
	v_mul_f32_e32 v62, v68, v62
	v_mul_f32_e32 v63, v68, v63
	v_mul_f32_e32 v64, v68, v64
	v_mul_f32_e32 v65, v68, v65
	v_mul_f32_e32 v66, v68, v66
	v_mul_f32_e32 v67, v68, v67
	ds_write2st64_b32 v7, v60, v61 offset1:32
	ds_write2st64_b32 v7, v62, v63 offset0:64 offset1:96
	ds_write2st64_b32 v7, v64, v65 offset0:128 offset1:160
	ds_write2st64_b32 v7, v66, v67 offset0:192 offset1:224
